# speedup vs baseline: 1.0423x; 1.0423x over previous
_Z6gat_k2PKDF16_S0_S0_PKfPf:
	s_load_dwordx8 s[4:11], s[0:1], 0x0
	s_load_dwordx2 s[12:13], s[0:1], 0x20
	v_readfirstlane_b32 s14, v0
	v_and_b32_e32 v46, 63, v0
	v_lshlrev_b32_e32 v1, 4, v46
	s_and_b32 s16, s2, 1
	s_bfe_u32 s17, s2, 0x60003
	s_lshr_b32 s18, s2, 1
	s_lshr_b32 s15, s14, 6
	s_lshl_b32 s19, s16, 19
	s_lshl_b32 s23, s15, 16
	s_add_u32 s19, s19, s23
	s_lshl_b32 s23, s15, 11
	v_add_u32_e32 v47, s23, v1
	v_and_b32_e32 v44, 31, v0
	v_lshlrev_b32_e32 v45, 2, v44
	s_lshl_b32 s23, s18, 8
	v_add_u32_e32 v45, s23, v45
	s_waitcnt lgkmcnt(0)
	global_load_dword v42, v45, s[10:11]
	global_load_dword v43, v45, s[10:11] offset:128
	global_load_dwordx4 v[48:51], v47, s[6:7]
	global_load_dwordx4 v[52:55], v47, s[6:7] offset:1024
	global_load_dwordx4 v[56:59], v47, s[8:9]
	global_load_dwordx4 v[60:63], v47, s[8:9] offset:1024
	s_add_u32 s20, s4, s19
	s_addc_u32 s21, s5, 0
	s_add_u32 s23, s17, 0
	s_and_b32 s23, s23, 63
	s_lshl_b32 s23, s23, 10
	s_add_u32 s24, s20, s23
	s_addc_u32 s25, s21, 0
	global_load_dwordx4 v[64:67], v1, s[24:25]
	s_add_u32 s23, s17, 1
	s_and_b32 s23, s23, 63
	s_lshl_b32 s23, s23, 10
	s_add_u32 s24, s20, s23
	s_addc_u32 s25, s21, 0
	global_load_dwordx4 v[68:71], v1, s[24:25]
	s_add_u32 s23, s17, 2
	s_and_b32 s23, s23, 63
	s_lshl_b32 s23, s23, 10
	s_add_u32 s24, s20, s23
	s_addc_u32 s25, s21, 0
	global_load_dwordx4 v[72:75], v1, s[24:25]
	s_add_u32 s23, s17, 3
	s_and_b32 s23, s23, 63
	s_lshl_b32 s23, s23, 10
	s_add_u32 s24, s20, s23
	s_addc_u32 s25, s21, 0
	global_load_dwordx4 v[76:79], v1, s[24:25]
	s_add_u32 s23, s17, 4
	s_and_b32 s23, s23, 63
	s_lshl_b32 s23, s23, 10
	s_add_u32 s24, s20, s23
	s_addc_u32 s25, s21, 0
	global_load_dwordx4 v[80:83], v1, s[24:25]
	s_add_u32 s23, s17, 5
	s_and_b32 s23, s23, 63
	s_lshl_b32 s23, s23, 10
	s_add_u32 s24, s20, s23
	s_addc_u32 s25, s21, 0
	global_load_dwordx4 v[84:87], v1, s[24:25]
	s_add_u32 s23, s17, 6
	s_and_b32 s23, s23, 63
	s_lshl_b32 s23, s23, 10
	s_add_u32 s24, s20, s23
	s_addc_u32 s25, s21, 0
	global_load_dwordx4 v[88:91], v1, s[24:25]
	s_add_u32 s23, s17, 7
	s_and_b32 s23, s23, 63
	s_lshl_b32 s23, s23, 10
	s_add_u32 s24, s20, s23
	s_addc_u32 s25, s21, 0
	global_load_dwordx4 v[92:95], v1, s[24:25]
	v_mov_b32_e32 v2, 0
	v_mov_b32_e32 v3, 0
	v_mov_b32_e32 v4, 0
	v_mov_b32_e32 v5, 0
	v_mov_b32_e32 v6, 0
	v_mov_b32_e32 v7, 0
	v_mov_b32_e32 v8, 0
	v_mov_b32_e32 v9, 0
	v_mov_b32_e32 v10, 0
	v_mov_b32_e32 v11, 0
	v_mov_b32_e32 v12, 0
	v_mov_b32_e32 v13, 0
	v_mov_b32_e32 v14, 0
	v_mov_b32_e32 v15, 0
	v_mov_b32_e32 v16, 0
	v_mov_b32_e32 v17, 0
	v_mov_b32_e32 v18, 0
	v_mov_b32_e32 v19, 0
	v_mov_b32_e32 v20, 0
	v_mov_b32_e32 v21, 0
	v_mov_b32_e32 v22, 0
	v_mov_b32_e32 v23, 0
	v_mov_b32_e32 v24, 0
	v_mov_b32_e32 v25, 0
	v_mov_b32_e32 v26, 0
	v_mov_b32_e32 v27, 0
	v_mov_b32_e32 v28, 0
	v_mov_b32_e32 v29, 0
	v_mov_b32_e32 v30, 0
	v_mov_b32_e32 v31, 0
	v_mov_b32_e32 v32, 0
	v_mov_b32_e32 v33, 0
	v_mov_b32_e32 v34, 0
	v_mov_b32_e32 v35, 0
	v_mov_b32_e32 v36, 0
	v_mov_b32_e32 v37, 0
	v_mov_b32_e32 v38, 0
	v_mov_b32_e32 v39, 0
	v_mov_b32_e32 v40, 0
	v_mov_b32_e32 v41, 0
	v_lshrrev_b32_e32 v44, 1, v46
	v_subrev_u32_e32 v44, s17, v44
	v_and_b32_e32 v44, 63, v44
	v_lshlrev_b32_e32 v44, 5, v44
	v_and_b32_e32 v45, 1, v46
	v_lshl_or_b32 v44, v45, 4, v44
	v_xor_b32_e32 v45, 0x400, v44
	s_mul_i32 s23, s15, 0x1900
	v_add_u32_e32 v44, s23, v44
	v_add_u32_e32 v45, s23, v45
	v_add_u32_e32 v47, s23, v1
	ds_write_b128 v47, v[34:37] offset:4096
	ds_write_b128 v47, v[34:37] offset:5120
	s_waitcnt vmcnt(8)
	ds_write_b128 v44, v[48:51]
	ds_write_b128 v45, v[52:55]
	ds_write_b128 v44, v[56:59] offset:2048
	ds_write_b128 v45, v[60:63] offset:2048
	v_cvt_f16_f32_e32 v42, v42
	v_cvt_f16_f32_e32 v43, v43
	s_mov_b32 s28, 0x5040100
	v_perm_b32 v42, v42, v42, s28
	v_perm_b32 v43, v43, v43, s28
	v_lshrrev_b32_e32 v44, 5, v46
	v_and_b32_e32 v45, 15, v46
	v_bfe_u32 v47, v46, 4, 1
	v_cmp_eq_u32_e32 vcc, v45, v47
	v_lshlrev_b32_e32 v44, 4, v44
	v_add_u32_e32 v46, s23, v44
	v_add_u32_e32 v45, 0x800, v46
	v_mov_b32_e32 v47, s23
	v_add_u32_e32 v47, 0x1000, v47
	v_cndmask_b32_e32 v47, v47, v45, vcc
	s_waitcnt lgkmcnt(0)
	ds_read_b128 v[144:147], v46
	ds_read_b128 v[148:151], v46 offset:32
	ds_read_b128 v[160:163], v47
	ds_read_b128 v[152:155], v46 offset:64
	ds_read_b128 v[164:167], v47 offset:32
	s_add_u32 s27, s17, 8
	s_lshl_b32 s27, s27, 10
	s_add_u32 s29, s17, 63
	s_lshl_b32 s29, s29, 10
	s_movk_i32 s28, 0x400
	s_mov_b32 s26, 0
	s_waitcnt lgkmcnt(4)
	v_pk_max_u16 v128, v144, v42
	v_pk_max_u16 v129, v145, v42
	v_pk_max_u16 v130, v146, v42
	v_pk_max_u16 v131, v147, v42
	v_pk_max_u16 v136, v144, v43
	v_pk_max_u16 v137, v145, v43
	v_pk_max_u16 v138, v146, v43
	v_pk_max_u16 v139, v147, v43
	s_nop 1
.Lk2_loop:
	s_and_b32 s23, s27, 0xfc00
	s_add_u32 s24, s20, s23
	s_addc_u32 s25, s21, 0
	s_add_u32 s27, s27, s28
	s_waitcnt vmcnt(7)
	v_mfma_f32_32x32x16_f16 v[2:17], v[64:67], v[128:131], v[2:17]
	s_waitcnt lgkmcnt(3)
	v_pk_max_u16 v132, v148, v42
	v_pk_max_u16 v133, v149, v42
	v_pk_max_u16 v134, v150, v42
	v_pk_max_u16 v135, v151, v42
	v_mfma_f32_32x32x16_f16 v[18:33], v[64:67], v[136:139], v[18:33]
	v_pk_max_u16 v140, v148, v43
	v_pk_max_u16 v141, v149, v43
	v_pk_max_u16 v142, v150, v43
	v_pk_max_u16 v143, v151, v43
	s_waitcnt lgkmcnt(2)
	v_mfma_f32_16x16x32_f16 v[34:37], v[160:163], v[128:131], v[34:37]
	global_load_dwordx4 v[64:67], v1, s[24:25]
	ds_read_b128 v[156:159], v46 offset:96
	ds_read_b128 v[168:171], v47 offset:64
	v_mfma_f32_16x16x32_f16 v[38:41], v[160:163], v[136:139], v[38:41]
	s_and_b32 s23, s27, 0xfc00
	s_add_u32 s24, s20, s23
	s_addc_u32 s25, s21, 0
	s_add_u32 s27, s27, s28
	s_waitcnt vmcnt(7)
	v_mfma_f32_32x32x16_f16 v[2:17], v[68:71], v[132:135], v[2:17]
	s_waitcnt lgkmcnt(3)
	v_pk_max_u16 v128, v152, v42
	v_pk_max_u16 v129, v153, v42
	v_pk_max_u16 v130, v154, v42
	v_pk_max_u16 v131, v155, v42
	v_mfma_f32_32x32x16_f16 v[18:33], v[68:71], v[140:143], v[18:33]
	v_pk_max_u16 v136, v152, v43
	v_pk_max_u16 v137, v153, v43
	v_pk_max_u16 v138, v154, v43
	v_pk_max_u16 v139, v155, v43
	s_waitcnt lgkmcnt(2)
	v_mfma_f32_16x16x32_f16 v[34:37], v[164:167], v[132:135], v[34:37]
	global_load_dwordx4 v[68:71], v1, s[24:25]
	ds_read_b128 v[144:147], v46 offset:128
	ds_read_b128 v[172:175], v47 offset:96
	v_mfma_f32_16x16x32_f16 v[38:41], v[164:167], v[140:143], v[38:41]
	s_and_b32 s23, s27, 0xfc00
	s_add_u32 s24, s20, s23
	s_addc_u32 s25, s21, 0
	s_add_u32 s27, s27, s28
	s_waitcnt vmcnt(7)
	v_mfma_f32_32x32x16_f16 v[2:17], v[72:75], v[128:131], v[2:17]
	s_waitcnt lgkmcnt(3)
	v_pk_max_u16 v132, v156, v42
	v_pk_max_u16 v133, v157, v42
	v_pk_max_u16 v134, v158, v42
	v_pk_max_u16 v135, v159, v42
	v_mfma_f32_32x32x16_f16 v[18:33], v[72:75], v[136:139], v[18:33]
	v_pk_max_u16 v140, v156, v43
	v_pk_max_u16 v141, v157, v43
	v_pk_max_u16 v142, v158, v43
	v_pk_max_u16 v143, v159, v43
	s_waitcnt lgkmcnt(2)
	v_mfma_f32_16x16x32_f16 v[34:37], v[168:171], v[128:131], v[34:37]
	global_load_dwordx4 v[72:75], v1, s[24:25]
	ds_read_b128 v[148:151], v46 offset:160
	ds_read_b128 v[160:163], v47 offset:128
	v_mfma_f32_16x16x32_f16 v[38:41], v[168:171], v[136:139], v[38:41]
	s_and_b32 s23, s27, 0xfc00
	s_add_u32 s24, s20, s23
	s_addc_u32 s25, s21, 0
	s_add_u32 s27, s27, s28
	s_waitcnt vmcnt(7)
	v_mfma_f32_32x32x16_f16 v[2:17], v[76:79], v[132:135], v[2:17]
	s_waitcnt lgkmcnt(3)
	v_pk_max_u16 v128, v144, v42
	v_pk_max_u16 v129, v145, v42
	v_pk_max_u16 v130, v146, v42
	v_pk_max_u16 v131, v147, v42
	v_mfma_f32_32x32x16_f16 v[18:33], v[76:79], v[140:143], v[18:33]
	v_pk_max_u16 v136, v144, v43
	v_pk_max_u16 v137, v145, v43
	v_pk_max_u16 v138, v146, v43
	v_pk_max_u16 v139, v147, v43
	s_waitcnt lgkmcnt(2)
	v_mfma_f32_16x16x32_f16 v[34:37], v[172:175], v[132:135], v[34:37]
	global_load_dwordx4 v[76:79], v1, s[24:25]
	ds_read_b128 v[152:155], v46 offset:192
	ds_read_b128 v[164:167], v47 offset:160
	v_mfma_f32_16x16x32_f16 v[38:41], v[172:175], v[140:143], v[38:41]
	s_and_b32 s23, s27, 0xfc00
	s_add_u32 s24, s20, s23
	s_addc_u32 s25, s21, 0
	s_add_u32 s27, s27, s28
	s_waitcnt vmcnt(7)
	v_mfma_f32_32x32x16_f16 v[2:17], v[80:83], v[128:131], v[2:17]
	s_waitcnt lgkmcnt(3)
	v_pk_max_u16 v132, v148, v42
	v_pk_max_u16 v133, v149, v42
	v_pk_max_u16 v134, v150, v42
	v_pk_max_u16 v135, v151, v42
	v_mfma_f32_32x32x16_f16 v[18:33], v[80:83], v[136:139], v[18:33]
	v_pk_max_u16 v140, v148, v43
	v_pk_max_u16 v141, v149, v43
	v_pk_max_u16 v142, v150, v43
	v_pk_max_u16 v143, v151, v43
	s_waitcnt lgkmcnt(2)
	v_mfma_f32_16x16x32_f16 v[34:37], v[160:163], v[128:131], v[34:37]
	global_load_dwordx4 v[80:83], v1, s[24:25]
	ds_read_b128 v[156:159], v46 offset:224
	ds_read_b128 v[168:171], v47 offset:192
	v_mfma_f32_16x16x32_f16 v[38:41], v[160:163], v[136:139], v[38:41]
	s_and_b32 s23, s27, 0xfc00
	s_add_u32 s24, s20, s23
	s_addc_u32 s25, s21, 0
	s_add_u32 s27, s27, s28
	s_waitcnt vmcnt(7)
	v_mfma_f32_32x32x16_f16 v[2:17], v[84:87], v[132:135], v[2:17]
	s_waitcnt lgkmcnt(3)
	v_pk_max_u16 v128, v152, v42
	v_pk_max_u16 v129, v153, v42
	v_pk_max_u16 v130, v154, v42
	v_pk_max_u16 v131, v155, v42
	v_mfma_f32_32x32x16_f16 v[18:33], v[84:87], v[140:143], v[18:33]
	v_pk_max_u16 v136, v152, v43
	v_pk_max_u16 v137, v153, v43
	v_pk_max_u16 v138, v154, v43
	v_pk_max_u16 v139, v155, v43
	s_waitcnt lgkmcnt(2)
	v_mfma_f32_16x16x32_f16 v[34:37], v[164:167], v[132:135], v[34:37]
	global_load_dwordx4 v[84:87], v1, s[24:25]
	ds_read_b128 v[144:147], v46 offset:256
	ds_read_b128 v[172:175], v47 offset:224
	v_mfma_f32_16x16x32_f16 v[38:41], v[164:167], v[140:143], v[38:41]
	s_and_b32 s23, s27, 0xfc00
	s_add_u32 s24, s20, s23
	s_addc_u32 s25, s21, 0
	s_add_u32 s27, s27, s28
	s_waitcnt vmcnt(7)
	v_mfma_f32_32x32x16_f16 v[2:17], v[88:91], v[128:131], v[2:17]
	s_waitcnt lgkmcnt(3)
	v_pk_max_u16 v132, v156, v42
	v_pk_max_u16 v133, v157, v42
	v_pk_max_u16 v134, v158, v42
	v_pk_max_u16 v135, v159, v42
	v_mfma_f32_32x32x16_f16 v[18:33], v[88:91], v[136:139], v[18:33]
	v_pk_max_u16 v140, v156, v43
	v_pk_max_u16 v141, v157, v43
	v_pk_max_u16 v142, v158, v43
	v_pk_max_u16 v143, v159, v43
	s_waitcnt lgkmcnt(2)
	v_mfma_f32_16x16x32_f16 v[34:37], v[168:171], v[128:131], v[34:37]
	global_load_dwordx4 v[88:91], v1, s[24:25]
	ds_read_b128 v[148:151], v46 offset:288
	ds_read_b128 v[160:163], v47 offset:256
	v_mfma_f32_16x16x32_f16 v[38:41], v[168:171], v[136:139], v[38:41]
	s_and_b32 s23, s27, 0xfc00
	s_add_u32 s24, s20, s23
	s_addc_u32 s25, s21, 0
	s_add_u32 s27, s27, s28
	s_waitcnt vmcnt(7)
	v_mfma_f32_32x32x16_f16 v[2:17], v[92:95], v[132:135], v[2:17]
	s_waitcnt lgkmcnt(3)
	v_pk_max_u16 v128, v144, v42
	v_pk_max_u16 v129, v145, v42
	v_pk_max_u16 v130, v146, v42
	v_pk_max_u16 v131, v147, v42
	v_mfma_f32_32x32x16_f16 v[18:33], v[92:95], v[140:143], v[18:33]
	v_pk_max_u16 v136, v144, v43
	v_pk_max_u16 v137, v145, v43
	v_pk_max_u16 v138, v146, v43
	v_pk_max_u16 v139, v147, v43
	s_waitcnt lgkmcnt(2)
	v_mfma_f32_16x16x32_f16 v[34:37], v[172:175], v[132:135], v[34:37]
	global_load_dwordx4 v[92:95], v1, s[24:25]
	ds_read_b128 v[152:155], v46 offset:320
	ds_read_b128 v[164:167], v47 offset:288
	v_mfma_f32_16x16x32_f16 v[38:41], v[172:175], v[140:143], v[38:41]
	s_add_u32 s26, s26, 1
	v_add_u32_e32 v46, 256, v46
	v_add_u32_e32 v47, 256, v47
	s_cmp_eq_u32 s26, 7
	s_cselect_b32 s27, s29, s27
	s_cselect_b32 s28, 0, s28
	s_cmp_lt_u32 s26, 8
	s_cbranch_scc1 .Lk2_loop
	v_and_b32_e32 v48, 63, v0
	v_lshrrev_b32_e32 v49, 5, v48
	v_and_b32_e32 v50, 31, v0
	s_lshl_b32 s23, s15, 4
	v_add_u32_e32 v49, s23, v49
	v_mul_u32_u24_e32 v49, 0x210, v49
	v_lshl_add_u32 v49, v50, 4, v49
	v_cmp_gt_u32_e32 vcc, 16, v48
	s_waitcnt vmcnt(0) lgkmcnt(0)
	s_barrier
	ds_write_b128 v49, v[2:5]
	ds_write_b128 v49, v[18:21] offset:4224
	ds_write_b128 v49, v[6:9] offset:1056
	ds_write_b128 v49, v[22:25] offset:5280
	ds_write_b128 v49, v[10:13] offset:2112
	ds_write_b128 v49, v[26:29] offset:6336
	ds_write_b128 v49, v[14:17] offset:3168
	ds_write_b128 v49, v[30:33] offset:7392
	s_and_saveexec_b64 s[2:3], vcc
	s_cbranch_execz .Lk2_nodred
	v_lshlrev_b32_e32 v51, 2, v48
	s_lshl_b32 s23, s15, 8
	v_add_u32_e32 v51, s23, v51
	v_add_u32_e32 v51, 0x10800, v51
	ds_write2_b32 v51, v34, v35 offset1:16
	ds_write2_b32 v51, v38, v39 offset0:32 offset1:48
.Lk2_nodred:
	s_or_b64 exec, exec, s[2:3]
	s_waitcnt lgkmcnt(0)
	s_barrier
	v_lshrrev_b32_e32 v5, 3, v0
	v_and_b32_e32 v4, 7, v0
	v_lshrrev_b32_e32 v1, 8, v0
	v_bfe_u32 v0, v0, 3, 5
	v_lshlrev_b32_e32 v2, 2, v0
	v_lshl_or_b32 v7, v1, 7, v2
	v_mul_u32_u24_e32 v1, 0x1080, v1
	v_mul_u32_u24_e32 v2, 0x210, v4
	v_lshlrev_b32_e32 v0, 4, v0
	v_mov_b32_e32 v6, 0
	s_mov_b32 s2, 8
	v_add3_u32 v8, v1, v2, v0
	v_mov_b32_e32 v0, 0
	v_mov_b32_e32 v1, v6
	v_mov_b32_e32 v2, 0
	v_mov_b32_e32 v3, v6
.Lk2_red:
	ds_read_b128 v[10:13], v8
	ds_read_b128 v[14:17], v8 offset:8448
	v_add_u32_e32 v9, 0x10800, v7
	v_add_u32_e32 v26, 0x10900, v7
	v_add_u32_e32 v27, 0x10a00, v7
	v_add_u32_e32 v28, 0x10b00, v7
	ds_read_b128 v[18:21], v8 offset:16896
	ds_read_b128 v[22:25], v8 offset:25344
	ds_read_b32 v9, v9
	ds_read_b32 v26, v26
	ds_read_b32 v27, v27
	ds_read_b32 v28, v28
	s_waitcnt lgkmcnt(7)
	v_pk_add_f32 v[2:3], v[2:3], v[12:13]
	v_pk_add_f32 v[0:1], v[0:1], v[10:11]
	s_waitcnt lgkmcnt(3)
	v_add_f32_e32 v6, v6, v9
	v_pk_add_f32 v[2:3], v[2:3], v[16:17]
	v_pk_add_f32 v[0:1], v[0:1], v[14:15]
	s_waitcnt lgkmcnt(2)
	v_add_f32_e32 v6, v6, v26
	s_add_i32 s2, s2, -4
	v_pk_add_f32 v[2:3], v[2:3], v[20:21]
	v_pk_add_f32 v[0:1], v[0:1], v[18:19]
	s_waitcnt lgkmcnt(1)
	v_add_f32_e32 v6, v6, v27
	v_add_u32_e32 v7, 0x400, v7
	v_add_u32_e32 v8, 0x8400, v8
	s_cmp_eq_u32 s2, 0
	v_pk_add_f32 v[2:3], v[2:3], v[24:25]
	v_pk_add_f32 v[0:1], v[0:1], v[22:23]
	s_waitcnt lgkmcnt(0)
	v_add_f32_e32 v6, v6, v28
	s_cbranch_scc0 .Lk2_red
	v_div_scale_f32 v7, s[2:3], v6, v6, 1.0
	v_rcp_f32_e32 v8, v7
	v_div_scale_f32 v9, vcc, 1.0, v6, 1.0
	s_mov_b32 s3, 0
	v_fma_f32 v10, -v7, v8, 1.0
	v_fmac_f32_e32 v8, v10, v8
	v_mul_f32_e32 v10, v9, v8
	v_fma_f32 v11, -v7, v10, v9
	v_fmac_f32_e32 v10, v11, v8
	v_fma_f32 v7, -v7, v10, v9
	v_div_fmas_f32 v7, v7, v8, v10
	v_div_fixup_f32 v6, v7, v6, 1.0
	v_pk_mul_f32 v[2:3], v[2:3], v[6:7] op_sel_hi:[1,0]
	v_pk_mul_f32 v[0:1], v[0:1], v[6:7] op_sel_hi:[1,0]
	s_lshl_b32 s4, s18, 6
	v_or_b32_e32 v6, s4, v5
	v_mov_b32_e32 v7, 0
	v_lshlrev_b64 v[8:9], 8, v[6:7]
	v_lshl_add_u64 v[8:9], s[12:13], 0, v[8:9]
	s_lshl_b32 s2, s16, 7
	v_lshl_add_u64 v[8:9], v[8:9], 0, s[2:3]
	v_lshlrev_b32_e32 v6, 4, v4
	v_lshl_add_u64 v[4:5], v[8:9], 0, v[6:7]
	global_store_dwordx4 v[4:5], v[0:3], off
	s_endpgm

	.amdhsa_kernel _Z6gat_k2PKDF16_S0_S0_PKfPf
		.amdhsa_group_segment_fixed_size 71680
		.amdhsa_private_segment_fixed_size 0
		.amdhsa_kernarg_size 40
		.amdhsa_user_sgpr_count 2
		.amdhsa_user_sgpr_dispatch_ptr 0
		.amdhsa_user_sgpr_queue_ptr 0
		.amdhsa_user_sgpr_kernarg_segment_ptr 1
		.amdhsa_user_sgpr_dispatch_id 0
		.amdhsa_user_sgpr_kernarg_preload_length 0
		.amdhsa_user_sgpr_kernarg_preload_offset 0
		.amdhsa_user_sgpr_private_segment_size 0
		.amdhsa_uses_dynamic_stack 0
		.amdhsa_enable_private_segment 0
		.amdhsa_system_sgpr_workgroup_id_x 1
		.amdhsa_system_sgpr_workgroup_id_y 0
		.amdhsa_system_sgpr_workgroup_id_z 0
		.amdhsa_system_sgpr_workgroup_info 0
		.amdhsa_system_vgpr_workitem_id 0
		.amdhsa_next_free_vgpr 176
		.amdhsa_next_free_sgpr 96
		.amdhsa_accum_offset 176
		.amdhsa_reserve_vcc 1
		.amdhsa_float_round_mode_32 0
		.amdhsa_float_round_mode_16_64 0
		.amdhsa_float_denorm_mode_32 3
		.amdhsa_float_denorm_mode_16_64 3
		.amdhsa_dx10_clamp 1
		.amdhsa_ieee_mode 1
		.amdhsa_fp16_overflow 0
		.amdhsa_tg_split 0
		.amdhsa_exception_fp_ieee_invalid_op 0
		.amdhsa_exception_fp_denorm_src 0
		.amdhsa_exception_fp_ieee_div_zero 0
		.amdhsa_exception_fp_ieee_overflow 0
		.amdhsa_exception_fp_ieee_underflow 0
		.amdhsa_exception_fp_ieee_inexact 0
		.amdhsa_exception_int_div_zero 0
	.end_amdhsa_kernel

amdhsa.kernels:
  - .agpr_count:     32
    .args:
      - .actual_access:  read_only
        .address_space:  global
        .offset:         0
        .size:           8
        .value_kind:     global_buffer
      - .actual_access:  read_only
        .address_space:  global
        .offset:         8
        .size:           8
        .value_kind:     global_buffer
      - .actual_access:  read_only
        .address_space:  global
        .offset:         16
        .size:           8
        .value_kind:     global_buffer
      - .actual_access:  read_only
        .address_space:  global
        .offset:         24
        .size:           8
        .value_kind:     global_buffer
      - .actual_access:  write_only
        .address_space:  global
        .offset:         32
        .size:           8
        .value_kind:     global_buffer
      - .actual_access:  write_only
        .address_space:  global
        .offset:         40
        .size:           8
        .value_kind:     global_buffer
      - .actual_access:  write_only
        .address_space:  global
        .offset:         48
        .size:           8
        .value_kind:     global_buffer
      - .actual_access:  write_only
        .address_space:  global
        .offset:         56
        .size:           8
        .value_kind:     global_buffer
    .group_segment_fixed_size: 68352
    .kernarg_segment_align: 8
    .kernarg_segment_size: 64
    .language:       OpenCL C
    .language_version:
      - 2
      - 0
    .max_flat_workgroup_size: 256
    .name:           _Z6gat_k1PKfS0_S0_S0_PDF16_S1_S1_Pf
    .private_segment_fixed_size: 0
    .sgpr_count:     18
    .sgpr_spill_count: 0
    .symbol:         _Z6gat_k1PKfS0_S0_S0_PDF16_S1_S1_Pf.kd
    .uniform_work_group_size: 1
    .uses_dynamic_stack: false
    .vgpr_count:     156
    .vgpr_spill_count: 0
    .wavefront_size: 64
  - .agpr_count:     0
    .args:
      - .actual_access:  read_only
        .address_space:  global
        .offset:         0
        .size:           8
        .value_kind:     global_buffer
      - .actual_access:  read_only
        .address_space:  global
        .offset:         8
        .size:           8
        .value_kind:     global_buffer
      - .actual_access:  read_only
        .address_space:  global
        .offset:         16
        .size:           8
        .value_kind:     global_buffer
      - .actual_access:  read_only
        .address_space:  global
        .offset:         24
        .size:           8
        .value_kind:     global_buffer
      - .actual_access:  write_only
        .address_space:  global
        .offset:         32
        .size:           8
        .value_kind:     global_buffer
    .group_segment_fixed_size: 71680
    .kernarg_segment_align: 8
    .kernarg_segment_size: 40
    .language:       OpenCL C
    .language_version:
      - 2
      - 0
    .max_flat_workgroup_size: 512
    .name:           _Z6gat_k2PKDF16_S0_S0_PKfPf
    .private_segment_fixed_size: 0
    .sgpr_count:     24
    .sgpr_spill_count: 0
    .symbol:         _Z6gat_k2PKDF16_S0_S0_PKfPf.kd
    .uniform_work_group_size: 1
    .uses_dynamic_stack: false
    .vgpr_count:     176
    .vgpr_spill_count: 0
    .wavefront_size: 64
